# four (was three) conversion items per wave in the attention context-tail barrier
# speedup vs baseline: 1.0066x; 1.0030x over previous
.Lcvt_post:
	s_mov_b64 exec, -1
	s_waitcnt lgkmcnt(0)
	s_cmp_lg_u32 s92, 0x100
	s_cbranch_scc1 .Lcvt_ret
	v_lshrrev_b32_e32 v2, 6, v0
	v_and_b32_e32 v3, 63, v0
	s_nop 0
	v_readfirstlane_b32 s25, v2
	s_nop 3
	v_lshrrev_b32_e32 v4, 3, v3
	v_and_b32_e32 v5, 7, v3
	v_mul_u32_u24_e32 v7, 17, v4
	v_and_b32_e32 v8, 3, v3
	v_lshl_add_u32 v7, v8, 2, v7
	v_lshlrev_b32_e32 v7, 2, v7
	v_mul_u32_u24_e32 v8, 0x110, v5
	v_add_lshl_u32 v8, v8, v4, 2
	s_mul_i32 s17, s25, 0x2200
	v_add_u32_e32 v7, s17, v7
	v_add_u32_e32 v8, s17, v8
	v_lshlrev_b32_e32 v9, 10, v4
	v_lshl_add_u32 v9, v5, 4, v9
	v_add_u32_e32 v10, 0x2000, v9
	s_cmp_eq_u32 s31, 5
	s_cbranch_scc0 .Lcvt_t3
	s_cmp_ge_u32 s62, 3
	s_cbranch_scc1 .Lcvt_ret
	s_sub_i32 s27, s80, 16
	s_cmp_lt_i32 s27, 0
	s_cbranch_scc1 .Lcvt_ret
	s_mov_b32 s26, 4
	s_movk_i32 s30, 0
	s_movk_i32 s4, 6720
	s_mov_b32 s24, s62
	s_branch .Lcvt_go
.Lcvt_t3:
	s_cmp_eq_u32 s31, 3
	s_cbranch_scc0 .Lcvt_t10
	s_mov_b32 s24, s62
	s_sub_i32 s27, s63, 208
	s_cmp_lt_i32 s27, 0
	s_cbranch_scc1 .Lcvt_t3b
	s_mov_b32 s26, 3
	s_movk_i32 s30, 6720
	s_movk_i32 s4, 7728
	s_branch .Lcvt_go
.Lcvt_t3b:
	s_mov_b32 s27, s63
	s_mov_b32 s26, 1
	s_movk_i32 s30, 7728
	s_movk_i32 s4, 9184
	s_branch .Lcvt_go
.Lcvt_t10:
	s_cmp_eq_u32 s31, 10
	s_cbranch_scc0 .Lcvt_lock
	s_cmp_ge_u32 s62, 3
	s_cbranch_scc1 .Lcvt_ret
	s_add_i32 s24, s62, 1
	s_sub_i32 s27, s63, 136
	s_cmp_lt_i32 s27, 0
	s_cbranch_scc1 .Lcvt_t10b
	s_mov_b32 s26, 4
	s_movk_i32 s30, 9184
	s_movk_i32 s4, 12544
	s_branch .Lcvt_go
.Lcvt_t10b:
	s_mov_b32 s27, s63
	s_mov_b32 s26, 1
	s_movk_i32 s30, 12544
	s_movk_i32 s4, 13496

.Lcvt_lk_c:
	s_mov_b32 s26, 2199
	s_mov_b32 s4, 15392
	s_cmp_eq_u32 s27, 1
	s_cselect_b32 s26, 1385, s26
	s_cselect_b32 s4, 11080, s4
	s_cmp_eq_u32 s27, 2
	s_cselect_b32 s26, 1385, s26
	s_cselect_b32 s4, 11080, s4
	s_cmp_eq_u32 s27, 3
	s_cselect_b32 s26, 2225, s26
	s_cselect_b32 s4, 17800, s4
	s_mul_i32 s30, s24, s26
	s_add_i32 s24, s30, s26
	s_min_u32 s4, s4, s24
	s_mul_i32 s26, s80, 7
	s_add_i32 s26, s26, s25
	s_add_i32 s26, s26, -1
	s_add_i32 s30, s30, s26
	s_mov_b32 s26, 2
	s_movk_i32 s25, 0x700
.Lcvt_item:
	s_cmp_ge_u32 s30, s4
	s_cbranch_scc1 .Lcvt_ret
	s_mov_b32 s6, s27
	s_mov_b32 s5, s30
	s_cmp_eq_u32 s25, 1
	s_cbranch_scc1 .Lcvt_dec
	s_cmp_eq_u32 s27, 3
	s_cbranch_scc1 .Lcvt_m3
	s_mov_b32 s24, 9184
	s_cmp_eq_u32 s27, 0
	s_cselect_b32 s24, s24, 13496
	s_add_i32 s5, s5, s24
	s_branch .Lcvt_dec
.Lcvt_m3:
	s_cmp_lt_u32 s5, 6720
	s_cbranch_scc1 .Lcvt_dec
	s_add_i32 s5, s5, 6776
